# P4 row blocks: chunk gating on 128 workgroups (one 128-token block, 8 heads, LN statistics once), conversion split 64 converter workgroups + gating workgroups afterwards
# speedup vs baseline: 1.0083x; 1.0013x over previous
; #define LBAR() do { asm volatile("s_waitcnt lgkmcnt(0)" ::: "memory"); __builtin_amdgcn_s_barrier(); asm volatile("" ::: "memory"); } while (0)
; __global__ void __launch_bounds__(NTHREADS, 2) fwd(Args args) {
;     ...
;             if (bid < 64 + NCMB) {
;                 for (int i = tid; i < 1024; i += NTHREADS) { gn[i] = cm_norm_g[i]; bn[i] = cm_norm_b[i]; bsl[i] = cm_b_s[i]; }
;                 LBAR();
;                 for (int u = bid - 64; u < NBATCH * 32 * 2; u += NCMB) {
;                     const int r0 = (u >> 1) * 128, h0 = (u & 1) * 4, r16 = lane & 15, q4 = lane >> 4;
; #pragma unroll 1
;                     for (int qb = 0; qb < 16; qb += 8) {
.LBB0_435:
	s_cmp_lt_i32 s90, 5
	s_cselect_b64 s[2:3], -1, 0
	s_add_u32 s10, s88, 0x4f600000
	s_addc_u32 s11, s89, 0
	s_add_u32 s12, s88, 0x4b600000
	s_addc_u32 s13, s89, 0
	s_add_u32 s16, s88, 0x63a00000
	s_addc_u32 s17, s89, 0
	s_and_b64 s[0:1], s[2:3], s[0:1]
	s_andn2_b64 vcc, exec, s[0:1]
	s_cbranch_vccnz .LBB0_520
	s_cmp_gt_i32 s94, 63
	s_mov_b64 s[4:5], -1
	s_cbranch_scc0 .LBB0_479
	s_cmpk_gt_u32 s94, 0xbf
	s_cbranch_scc1 .LBB0_464
	s_waitcnt vmcnt(0)
	v_add_u32_e32 v2, 0, v194
	v_mov_b32_e32 v195, 0
	v_add_u32_e32 v8, 0x400, v2
	v_lshl_add_u64 v[2:3], s[70:71], 0, v[194:195]
	v_lshl_add_u64 v[4:5], s[72:73], 0, v[194:195]
	v_lshl_add_u64 v[6:7], s[76:77], 0, v[194:195]
	s_mov_b64 s[4:5], 0
	s_mov_b64 s[6:7], 0x800
	v_mov_b32_e32 v9, v221
.LBB0_439:
	global_load_dword v10, v[2:3], off
	global_load_dword v11, v[4:5], off
	global_load_dword v12, v[6:7], off
	v_add_co_u32_e32 v9, vcc, 0x200, v9
	s_xor_b64 s[2:3], vcc, -1
	s_and_b64 s[2:3], exec, s[2:3]
	v_lshl_add_u64 v[2:3], v[2:3], 0, s[6:7]
	v_lshl_add_u64 v[4:5], v[4:5], 0, s[6:7]
	v_lshl_add_u64 v[6:7], v[6:7], 0, s[6:7]
	s_or_b64 s[4:5], s[2:3], s[4:5]
	s_waitcnt vmcnt(1)
	ds_write2st64_b32 v8, v10, v11 offset1:16
	s_waitcnt vmcnt(0)
	ds_write_b32 v8, v12 offset:8192
	v_add_u32_e32 v8, 0x800, v8
	s_andn2_b64 exec, exec, s[4:5]
	s_cbranch_execnz .LBB0_439
	s_or_b64 exec, exec, s[4:5]
	v_mbcnt_lo_u32_b32 v2, -1, 0
	v_mbcnt_hi_u32_b32 v2, -1, v2
	v_and_b32_e32 v3, 64, v2
	v_add_u32_e32 v3, 64, v3
	v_xor_b32_e32 v4, 1, v2
	v_cmp_lt_i32_e32 vcc, v4, v3
	v_readlane_b32 s14, v246, 21
	v_and_b32_e32 v112, 15, v0
	v_cndmask_b32_e32 v4, v2, v4, vcc
	v_lshlrev_b32_e32 v113, 2, v4
	v_xor_b32_e32 v4, 2, v2
	v_cmp_lt_i32_e32 vcc, v4, v3
	s_lshl_b32 s2, s14, 4
	s_movk_i32 s4, 0x110
	v_cndmask_b32_e32 v4, v2, v4, vcc
	v_lshlrev_b32_e32 v114, 2, v4
	v_xor_b32_e32 v4, 4, v2
	v_cmp_lt_i32_e32 vcc, v4, v3
	s_sub_i32 s3, s94, 64
	s_lshl_b32 s3, s3, 1
	v_lshrrev_b32_e32 v5, 1, v220
	v_cndmask_b32_e32 v4, v2, v4, vcc
	v_lshlrev_b32_e32 v115, 2, v4
	v_xor_b32_e32 v4, 8, v2
	v_cmp_lt_i32_e32 vcc, v4, v3
	v_lshlrev_b32_e32 v60, 5, v220
	v_mov_b32_e32 v61, 0
	v_cndmask_b32_e32 v4, v2, v4, vcc
	v_lshlrev_b32_e32 v116, 2, v4
	v_xor_b32_e32 v4, 16, v2
	v_cmp_lt_i32_e32 vcc, v4, v3
	v_lshl_add_u64 v[62:63], s[62:63], 0, v[60:61]
	v_or_b32_e32 v9, 0x400, v0
	v_cndmask_b32_e32 v4, v2, v4, vcc
	v_lshlrev_b32_e32 v117, 2, v4
	v_xor_b32_e32 v4, 32, v2
	v_cmp_lt_i32_e32 vcc, v4, v3
	v_or_b32_e32 v11, 0x600, v0
	v_or_b32_e32 v13, 0xa00, v0
	v_cndmask_b32_e32 v2, v2, v4, vcc
	v_lshlrev_b32_e32 v118, 2, v2
	v_and_b32_e32 v2, 0x7c, v194
	v_lshl_add_u32 v3, v2, 1, 0
	v_and_b32_e32 v2, 0x7f, v0
	v_lshl_add_u32 v119, v2, 3, 0
	v_mad_i32_i24 v6, v2, -6, v119
	v_and_b32_e32 v2, 48, v220
	v_or_b32_e32 v4, s2, v112
	v_add_u32_e32 v2, 0, v2
	v_mad_u64_u32 v[58:59], s[8:9], v4, s4, v[2:3]
	s_lshl_b32 s4, s94, 2
	s_add_i32 s20, s4, 0xffffff00
	s_lshl_b32 s20, s20, 1
	v_lshrrev_b32_e32 v4, 5, v0
	s_add_u32 s21, s74, 0x10000
	v_mul_u32_u24_e32 v7, 0x110, v4
	v_or_b32_e32 v4, 0x200, v0
	s_addc_u32 s22, s75, 0
	s_lshl_b32 s4, s94, 6
	v_lshrrev_b32_e32 v8, 5, v4
	v_lshrrev_b32_e32 v17, 4, v4
	s_add_i32 s23, s4, 0xfffff000
	s_lshl_b32 s23, s23, 1
	v_lshrrev_b32_e32 v4, 2, v4
	s_lshl_b32 s4, s14, 5
	v_and_b32_e32 v122, 0xe0, v4
	v_lshrrev_b32_e32 v4, 2, v0
	v_and_or_b32 v60, v5, 24, s4
	s_lshr_b32 s4, s51, 1
	v_and_b32_e32 v123, 0x60, v4
	v_lshl_add_u64 v[4:5], s[88:89], 0, v[60:61]
	s_mov_b64 s[8:9], 0x47600000
	s_and_b32 s4, s4, 0x7fffffe0
	v_or_b32_e32 v14, 0xe00, v0
	v_lshrrev_b32_e32 v15, 4, v0
	v_lshrrev_b32_e32 v19, 4, v9
	v_lshrrev_b32_e32 v21, 4, v11
	v_lshl_add_u64 v[64:65], v[4:5], 0, s[8:9]
	v_lshrrev_b32_e32 v4, 1, v0
	s_add_u32 s8, s88, s4
	s_waitcnt lgkmcnt(0)
	s_barrier
	v_lshrrev_b32_e32 v10, 5, v9
	v_lshrrev_b32_e32 v12, 5, v11
	v_lshrrev_b32_e32 v13, 5, v13
	v_lshrrev_b32_e32 v14, 5, v14
	v_and_b32_e32 v16, 24, v15
	v_or_b32_e32 v15, 7, v15
	v_and_b32_e32 v18, 56, v17
	v_or_b32_e32 v17, 7, v17
	v_and_b32_e32 v20, 0x58, v19
	v_or_b32_e32 v19, 7, v19
	v_and_b32_e32 v22, 0x78, v21
	v_or_b32_e32 v21, 7, v21
	v_and_b32_e32 v60, 24, v4
	s_addc_u32 s9, s89, 0
	v_mul_u32_u24_e32 v8, 0x110, v8
	v_mul_u32_u24_e32 v10, 0x110, v10
	v_mul_u32_u24_e32 v12, 0x110, v12
	v_mul_u32_u24_e32 v13, 0x110, v13
	v_mul_u32_u24_e32 v14, 0x110, v14
	v_mul_u32_u24_e32 v16, 0x110, v16
	v_mul_u32_u24_e32 v15, 0x110, v15
	v_mul_u32_u24_e32 v18, 0x110, v18
	v_mul_u32_u24_e32 v17, 0x110, v17
	v_mul_u32_u24_e32 v20, 0x110, v20
	v_mul_u32_u24_e32 v19, 0x110, v19
	v_mul_u32_u24_e32 v22, 0x110, v22
	v_mul_u32_u24_e32 v21, 0x110, v21
	v_mul_u32_u24_e32 v23, 0x110, v112
	v_lshrrev_b32_e32 v11, 2, v11
	v_lshrrev_b32_e32 v9, 2, v9
	v_lshl_add_u64 v[4:5], s[8:9], 0, v[60:61]
	s_mov_b64 s[8:9], 0x3c800000
	s_mov_b32 s5, 0
	v_cmp_eq_u32_e64 s[6:7], 0, v220
	v_lshlrev_b32_e32 v59, 2, v112
	v_and_b32_e32 v120, 0x1e0, v11
	v_and_b32_e32 v121, 0x160, v9
	v_or_b32_e32 v124, 0x70, v112
	v_or_b32_e32 v125, 0x60, v112
	v_or_b32_e32 v126, 0x50, v112
	v_or_b32_e32 v127, 64, v112
	v_or_b32_e32 v128, 48, v112
	v_or_b32_e32 v129, 32, v112
	v_or_b32_e32 v130, 16, v112
	v_lshl_add_u64 v[66:67], v[4:5], 0, s[8:9]
	s_movk_i32 s24, 0x2800
	v_mov_b32_e32 v131, 0x3727c5ac
	s_mov_b32 s25, 0xf800000
	v_mov_b32_e32 v132, 0x260
	v_add_u32_e32 v133, v3, v7
	v_add_u32_e32 v134, v3, v8
	v_add_u32_e32 v135, v3, v10
	v_add_u32_e32 v136, v3, v12
	v_add_u32_e32 v137, v3, v13
	v_add_u32_e32 v138, v3, v14
	v_add_u32_e32 v139, v6, v16
	v_add_u32_e32 v140, v6, v15
	v_add_u32_e32 v141, v6, v18
	v_add_u32_e32 v142, v6, v17
	v_add_u32_e32 v143, v6, v20
	v_add_u32_e32 v144, v6, v19
	v_add_u32_e32 v145, v6, v22
	v_add_u32_e32 v146, v6, v21
	s_mov_b32 s26, 0x3c800000
	v_add_u32_e32 v147, v2, v23
	v_mov_b32_e32 v148, 0x2800
	s_branch .LBB0_442
.LBB0_441:
	s_add_i32 s4, s3, 0x60
	s_addk_i32 s20, 0x180
	s_addk_i32 s23, 0x1800
	s_cmpk_gt_i32 s3, -1
	s_mov_b32 s3, s4
	s_cbranch_scc1 .LBB0_464

; #define LBAR() do { asm volatile("s_waitcnt lgkmcnt(0)" ::: "memory"); __builtin_amdgcn_s_barrier(); asm volatile("" ::: "memory"); } while (0)
; __global__ void __launch_bounds__(NTHREADS, 2) fwd(Args args) {
;     ...
;                     f32x4 wreg[8]; u32x4 vreg[4]; u32x2 ureg[8];
;     ...
;                     CM_LOAD(h0);
;                     LBAR();
; #pragma unroll 1
;                     for (int h = h0; h < h0 + 4; ++h) {
; #pragma unroll
;                         for (int tp = 0; tp < 8; ++tp) ureg[tp] = *(const u32x2*)(P + (size_t)(r0 + 16 * tp + r16) * NP + C_U + h * 128 + 16 * wave + 4 * q4);
.LBB0_460:
	s_bfe_u32 s4, s20, 0x10002
	s_lshl_b32 s8, s4, 18
	s_add_u32 s8, s21, s8
	s_addc_u32 s9, s22, 0
	s_and_b32 s18, s23, 0xffffff80
	s_lshl_b32 s14, s4, 10
	s_add_u32 s19, s88, s14
	s_addc_u32 s28, s89, 0
	s_lshl_b32 s15, s4, 2
	v_mov_b32_e32 v36, v0
	s_or_b32 s29, s15, 1
	s_lshl_b32 s15, s4, 11
	s_lshl_b32 s4, s3, 2
	s_and_b32 s33, s4, 4
	v_lshlrev_b32_e32 v2, 4, v36
	v_add_u32_e32 v37, 0x200, v36
	v_add_u32_e32 v44, 0x400, v36
	v_add_u32_e32 v46, 0x600, v36
	v_add_u32_e32 v18, 0x800, v36
	v_add_u32_e32 v20, 0xa00, v36
	v_add_u32_e32 v28, 0xc00, v36
	v_add_u32_e32 v30, 0xe00, v36
	v_and_b32_e32 v60, 0x1f0, v2
	v_ashrrev_i32_e32 v2, 5, v36
	s_waitcnt lgkmcnt(0)
	v_ashrrev_i32_e32 v4, 5, v37
	v_ashrrev_i32_e32 v10, 5, v44
	v_ashrrev_i32_e32 v12, 5, v46
	v_ashrrev_i32_e32 v18, 5, v18
	v_ashrrev_i32_e32 v20, 5, v20
	v_ashrrev_i32_e32 v28, 5, v28
	v_ashrrev_i32_e32 v30, 5, v30
	v_and_b32_e32 v34, 0x7f, v36
	s_lshl_b32 s4, s33, 7
	v_ashrrev_i32_e32 v3, 31, v2
	v_ashrrev_i32_e32 v5, 31, v4
	v_ashrrev_i32_e32 v11, 31, v10
	v_ashrrev_i32_e32 v13, 31, v12
	v_ashrrev_i32_e32 v19, 31, v18
	v_ashrrev_i32_e32 v21, 31, v20
	v_ashrrev_i32_e32 v29, 31, v28
	v_ashrrev_i32_e32 v31, 31, v30
	v_or_b32_e32 v38, s27, v34
	v_mov_b64_e32 v[34:35], s[62:63]
	v_lshl_add_u64 v[2:3], v[2:3], 0, s[4:5]
	v_lshl_add_u64 v[4:5], v[4:5], 0, s[4:5]
	v_lshl_add_u64 v[10:11], v[10:11], 0, s[4:5]
	v_lshl_add_u64 v[12:13], v[12:13], 0, s[4:5]
	v_lshl_add_u64 v[18:19], v[18:19], 0, s[4:5]
	v_lshl_add_u64 v[20:21], v[20:21], 0, s[4:5]
	v_lshl_add_u64 v[28:29], v[28:29], 0, s[4:5]
	v_lshl_add_u64 v[30:31], v[30:31], 0, s[4:5]
	v_mad_i64_i32 v[34:35], s[30:31], v38, s24, v[34:35]
	s_lshl_b32 s4, s33, 8
	v_lshl_add_u64 v[42:43], v[34:35], 0, s[4:5]
	v_ashrrev_i32_e32 v34, 4, v36
	v_ashrrev_i32_e32 v36, 4, v37
	v_ashrrev_i32_e32 v44, 4, v44
	v_ashrrev_i32_e32 v46, 4, v46
	v_and_b32_e32 v34, -8, v34
	v_and_b32_e32 v36, -8, v36
	v_and_b32_e32 v44, -8, v44
	v_and_b32_e32 v46, -8, v46
	v_lshl_add_u64 v[26:27], s[74:75], 0, v[60:61]
	v_lshlrev_b64 v[2:3], 9, v[2:3]
	v_lshlrev_b64 v[4:5], 9, v[4:5]
	v_lshlrev_b64 v[10:11], 9, v[10:11]
	v_lshlrev_b64 v[12:13], 9, v[12:13]
	v_lshlrev_b64 v[18:19], 9, v[18:19]
	v_lshlrev_b64 v[20:21], 9, v[20:21]
	v_lshlrev_b64 v[28:29], 9, v[28:29]
	v_lshlrev_b64 v[30:31], 9, v[30:31]
	v_ashrrev_i32_e32 v35, 31, v34
	v_ashrrev_i32_e32 v37, 31, v36
	v_ashrrev_i32_e32 v45, 31, v44
	v_ashrrev_i32_e32 v47, 31, v46
	v_lshl_add_u64 v[2:3], v[26:27], 0, v[2:3]
	v_lshl_add_u64 v[6:7], v[26:27], 0, v[4:5]
	v_lshl_add_u64 v[10:11], v[26:27], 0, v[10:11]
	v_lshl_add_u64 v[14:15], v[26:27], 0, v[12:13]
	v_lshl_add_u64 v[18:19], v[26:27], 0, v[18:19]
	v_lshl_add_u64 v[22:23], v[26:27], 0, v[20:21]
	v_lshl_add_u64 v[28:29], v[26:27], 0, v[28:29]
	v_lshl_add_u64 v[30:31], v[26:27], 0, v[30:31]
	v_lshl_add_u64 v[34:35], v[34:35], 1, v[42:43]
	v_lshl_add_u64 v[38:39], v[36:37], 1, v[42:43]
	v_lshl_add_u64 v[44:45], v[44:45], 1, v[42:43]
	v_lshl_add_u64 v[46:47], v[46:47], 1, v[42:43]
	global_load_dwordx4 v[2:5], v[2:3], off
	s_nop 0
	global_load_dwordx4 v[6:9], v[6:7], off
	s_nop 0
	global_load_dwordx4 v[10:13], v[10:11], off
	s_nop 0
	global_load_dwordx4 v[14:17], v[14:15], off
	s_nop 0
	global_load_dwordx4 v[18:21], v[18:19], off
	s_nop 0
	global_load_dwordx4 v[22:25], v[22:23], off
	s_nop 0
	global_load_dwordx4 v[26:29], v[28:29], off
	s_nop 0
	global_load_dwordx4 v[30:33], v[30:31], off
	s_nop 0
	global_load_dwordx4 v[34:37], v[34:35], off offset:2048
	s_nop 0
	global_load_dwordx4 v[38:41], v[38:39], off offset:2048
	s_nop 0
	global_load_dwordx4 v[42:45], v[44:45], off offset:2048
	s_nop 0
	global_load_dwordx4 v[46:49], v[46:47], off offset:2048
	v_or_b32_e32 v50, s18, v124
	v_ashrrev_i32_e32 v51, 31, v50
	v_lshlrev_b64 v[52:53], 12, v[50:51]
	v_or_b32_e32 v52, s14, v52
	v_mad_i64_i32 v[50:51], s[30:31], v50, s24, 0
	v_lshl_add_u64 v[54:55], v[64:65], 0, v[52:53]
	v_or_b32_e32 v52, s18, v125
	v_or_b32_e32 v50, s14, v50
	v_lshl_add_u64 v[80:81], v[66:67], 0, v[50:51]
	v_mad_i64_i32 v[50:51], s[30:31], v52, s24, 0
	v_or_b32_e32 v84, s18, v126
	v_or_b32_e32 v50, s14, v50
	v_lshl_add_u64 v[82:83], v[66:67], 0, v[50:51]
	v_mad_i64_i32 v[50:51], s[30:31], v84, s24, 0
	v_ashrrev_i32_e32 v85, 31, v84
	v_or_b32_e32 v86, s18, v127
	v_or_b32_e32 v50, s14, v50
	v_lshlrev_b64 v[68:69], 12, v[84:85]
	v_lshl_add_u64 v[84:85], v[66:67], 0, v[50:51]
	v_mad_i64_i32 v[50:51], s[30:31], v86, s24, 0
	v_ashrrev_i32_e32 v87, 31, v86
	v_or_b32_e32 v88, s18, v128
	v_or_b32_e32 v50, s14, v50
	v_lshlrev_b64 v[70:71], 12, v[86:87]
	v_lshl_add_u64 v[86:87], v[66:67], 0, v[50:51]
	v_mad_i64_i32 v[50:51], s[30:31], v88, s24, 0
	v_ashrrev_i32_e32 v89, 31, v88
	v_or_b32_e32 v90, s18, v129
	v_or_b32_e32 v50, s14, v50
	v_lshlrev_b64 v[72:73], 12, v[88:89]
	v_lshl_add_u64 v[88:89], v[66:67], 0, v[50:51]
	v_mad_i64_i32 v[50:51], s[30:31], v90, s24, 0
	v_ashrrev_i32_e32 v91, 31, v90
	v_or_b32_e32 v92, s18, v130
	v_or_b32_e32 v50, s14, v50
	v_lshlrev_b64 v[74:75], 12, v[90:91]
	v_or_b32_e32 v94, s18, v112
	v_lshl_add_u64 v[90:91], v[66:67], 0, v[50:51]
	v_mad_i64_i32 v[50:51], s[30:31], v92, s24, 0
	v_ashrrev_i32_e32 v53, 31, v52
	v_ashrrev_i32_e32 v93, 31, v92
	v_ashrrev_i32_e32 v95, 31, v94
	v_or_b32_e32 v50, s14, v50
	v_lshlrev_b64 v[56:57], 12, v[52:53]
	v_lshlrev_b64 v[76:77], 12, v[92:93]
	v_lshlrev_b64 v[78:79], 12, v[94:95]
	v_lshl_add_u64 v[92:93], v[66:67], 0, v[50:51]
	v_mad_i64_i32 v[50:51], s[30:31], v94, s24, 0
	s_waitcnt lgkmcnt(0)
	s_barrier
	v_or_b32_e32 v56, s14, v56
	v_or_b32_e32 v68, s14, v68
	v_or_b32_e32 v70, s14, v70
	v_or_b32_e32 v72, s14, v72
	v_or_b32_e32 v74, s14, v74
	v_or_b32_e32 v76, s14, v76
	v_or_b32_e32 v78, s14, v78
	v_or_b32_e32 v50, s14, v50
	s_add_i32 s4, s15, 0
	v_lshl_add_u64 v[56:57], v[64:65], 0, v[56:57]
	v_lshl_add_u64 v[68:69], v[64:65], 0, v[68:69]
	v_lshl_add_u64 v[70:71], v[64:65], 0, v[70:71]
	v_lshl_add_u64 v[72:73], v[64:65], 0, v[72:73]
	v_lshl_add_u64 v[74:75], v[64:65], 0, v[74:75]
	v_lshl_add_u64 v[76:77], v[64:65], 0, v[76:77]
	v_lshl_add_u64 v[78:79], v[64:65], 0, v[78:79]
	v_lshl_add_u64 v[94:95], v[66:67], 0, v[50:51]
	s_add_i32 s27, s33, 8
	s_mov_b64 s[14:15], 0
	s_branch .LBB0_462
; #define LAS __attribute__((address_space(3)))
; __device__ __forceinline__ unsigned pk2(float lo, float hi) { const f32v2 v = {lo, hi}; return __builtin_bit_cast(unsigned, __builtin_convertvector(v, bf16v2)); }
; __global__ void __launch_bounds__(NTHREADS, 2) fwd(Args args) {
;     ...
;                         f32x4 acc[8];
; #pragma unroll
;                         for (int tp = 0; tp < 8; ++tp) acc[tp] = (f32x4){0.f, 0.f, 0.f, 0.f};
; #pragma unroll
;                         for (int ks = 0; ks < 4; ++ks) { const bf16x8 a = *(const LAS bf16x8*)(VnT + (16 * wave + r16) * 136 + 32 * ks + 8 * q4);
; #pragma unroll
;                             for (int tp = 0; tp < 8; ++tp) { const bf16x8 bq = *(const LAS bf16x8*)(Ws + (16 * tp + r16) * 136 + 32 * ks + 8 * q4);
;                                 acc[tp] = __builtin_amdgcn_mfma_f32_16x16x32_bf16(a, bq, acc[tp], 0, 0, 0); } }
; #pragma unroll
;                         for (int tp = 0; tp < 8; ++tp) { const int pp = 16 * tp + r16, e0 = 16 * wave + 4 * q4; const float bs = bsl[h * 128 + pp]; const u32x2 uu = ureg[tp];
;                             u32x2 o; o.x = pk2(bflo(uu.x) * (acc[tp][0] + bs), bfhi(uu.x) * (acc[tp][1] + bs)); o.y = pk2(bflo(uu.y) * (acc[tp][2] + bs), bfhi(uu.y) * (acc[tp][3] + bs));
;                             *(u32x2*)(ACAT + (size_t)(r0 + pp) * D + h * 128 + e0) = o; }
.LBB0_461:
	s_waitcnt lgkmcnt(0)
	s_barrier
	ds_read_b128 v[50:53], v58 offset:48128
	ds_read_b128 v[150:153], v147 offset:13312
	ds_read_b128 v[154:157], v147 offset:17664
	ds_read_b128 v[178:181], v147 offset:43776
	ds_read_b128 v[158:161], v147 offset:22016
	ds_read_b128 v[162:165], v147 offset:26368
	ds_read_b128 v[166:169], v147 offset:30720
	ds_read_b128 v[170:173], v147 offset:35072
	ds_read_b128 v[174:177], v147 offset:39424
	s_waitcnt lgkmcnt(7)
	v_mfma_f32_16x16x32_bf16 v[150:153], v[50:53], v[150:153], 0
	v_add_u32_e32 v60, s4, v59
	v_add_u32_e32 v149, 0x2400, v60
	s_waitcnt lgkmcnt(6)
	v_mfma_f32_16x16x32_bf16 v[154:157], v[50:53], v[154:157], 0
	s_waitcnt lgkmcnt(4)
	v_mfma_f32_16x16x32_bf16 v[158:161], v[50:53], v[158:161], 0
	s_waitcnt lgkmcnt(3)
	v_mfma_f32_16x16x32_bf16 v[162:165], v[50:53], v[162:165], 0
	s_waitcnt lgkmcnt(2)
	v_mfma_f32_16x16x32_bf16 v[166:169], v[50:53], v[166:169], 0
	s_waitcnt lgkmcnt(1)
	v_mfma_f32_16x16x32_bf16 v[170:173], v[50:53], v[170:173], 0
	s_waitcnt lgkmcnt(0)
	v_mfma_f32_16x16x32_bf16 v[174:177], v[50:53], v[174:177], 0
	v_mfma_f32_16x16x32_bf16 v[50:53], v[50:53], v[178:181], 0
	ds_read_b128 v[178:181], v58 offset:48192
	ds_read_b128 v[182:185], v147 offset:13376
	s_waitcnt lgkmcnt(0)
	v_mfma_f32_16x16x32_bf16 v[150:153], v[178:181], v[182:185], v[150:153]
	ds_read_b128 v[182:185], v147 offset:17728
	s_waitcnt lgkmcnt(0)
	v_mfma_f32_16x16x32_bf16 v[154:157], v[178:181], v[182:185], v[154:157]
	ds_read_b128 v[182:185], v147 offset:22080
	s_waitcnt lgkmcnt(0)
	v_mfma_f32_16x16x32_bf16 v[158:161], v[178:181], v[182:185], v[158:161]
	ds_read_b128 v[182:185], v147 offset:26432
	s_waitcnt lgkmcnt(0)
	v_mfma_f32_16x16x32_bf16 v[162:165], v[178:181], v[182:185], v[162:165]
	ds_read_b128 v[182:185], v147 offset:30784
	s_waitcnt lgkmcnt(0)
	v_mfma_f32_16x16x32_bf16 v[166:169], v[178:181], v[182:185], v[166:169]
	ds_read_b128 v[182:185], v147 offset:35136
	s_waitcnt lgkmcnt(0)
	v_mfma_f32_16x16x32_bf16 v[170:173], v[178:181], v[182:185], v[170:173]
	ds_read_b128 v[182:185], v147 offset:39488
	s_waitcnt lgkmcnt(0)
	v_mfma_f32_16x16x32_bf16 v[174:177], v[178:181], v[182:185], v[174:177]
	ds_read_b128 v[182:185], v147 offset:43840
	s_waitcnt lgkmcnt(0)
	v_mfma_f32_16x16x32_bf16 v[50:53], v[178:181], v[182:185], v[50:53]
	ds_read_b128 v[178:181], v58 offset:48256
	ds_read_b128 v[182:185], v147 offset:13440
	s_waitcnt lgkmcnt(0)
	v_mfma_f32_16x16x32_bf16 v[150:153], v[178:181], v[182:185], v[150:153]
	ds_read_b128 v[182:185], v147 offset:17792
	s_waitcnt lgkmcnt(0)
	v_mfma_f32_16x16x32_bf16 v[154:157], v[178:181], v[182:185], v[154:157]
	ds_read_b128 v[182:185], v147 offset:22144
	s_waitcnt lgkmcnt(0)
	v_mfma_f32_16x16x32_bf16 v[158:161], v[178:181], v[182:185], v[158:161]
	ds_read_b128 v[182:185], v147 offset:26496
	s_waitcnt lgkmcnt(0)
	v_mfma_f32_16x16x32_bf16 v[162:165], v[178:181], v[182:185], v[162:165]
	ds_read_b128 v[182:185], v147 offset:30848
	s_waitcnt lgkmcnt(0)
	v_mfma_f32_16x16x32_bf16 v[166:169], v[178:181], v[182:185], v[166:169]
	ds_read_b128 v[182:185], v147 offset:35200
	s_waitcnt lgkmcnt(0)
	v_mfma_f32_16x16x32_bf16 v[170:173], v[178:181], v[182:185], v[170:173]
	ds_read_b128 v[182:185], v147 offset:39552
	s_waitcnt lgkmcnt(0)
	v_mfma_f32_16x16x32_bf16 v[174:177], v[178:181], v[182:185], v[174:177]
	ds_read_b128 v[182:185], v147 offset:43904
	s_waitcnt lgkmcnt(0)
	v_mfma_f32_16x16x32_bf16 v[50:53], v[178:181], v[182:185], v[50:53]
	ds_read_b128 v[178:181], v58 offset:48320
	ds_read_b128 v[182:185], v147 offset:13504
	s_waitcnt lgkmcnt(0)
	v_mfma_f32_16x16x32_bf16 v[150:153], v[178:181], v[182:185], v[150:153]
	ds_read_b128 v[182:185], v147 offset:17856
	s_waitcnt lgkmcnt(0)
	v_mfma_f32_16x16x32_bf16 v[154:157], v[178:181], v[182:185], v[154:157]
	ds_read_b128 v[182:185], v147 offset:22208
	s_waitcnt lgkmcnt(0)
	v_mfma_f32_16x16x32_bf16 v[158:161], v[178:181], v[182:185], v[158:161]
	ds_read_b128 v[182:185], v147 offset:26560
	s_waitcnt lgkmcnt(0)
	v_mfma_f32_16x16x32_bf16 v[162:165], v[178:181], v[182:185], v[162:165]
	ds_read_b128 v[182:185], v147 offset:30912
	s_waitcnt lgkmcnt(0)
	v_mfma_f32_16x16x32_bf16 v[166:169], v[178:181], v[182:185], v[166:169]
	ds_read_b128 v[182:185], v147 offset:35264
	s_waitcnt lgkmcnt(0)
	v_mfma_f32_16x16x32_bf16 v[170:173], v[178:181], v[182:185], v[170:173]
	ds_read_b128 v[182:185], v147 offset:39616
	s_waitcnt lgkmcnt(0)
	v_mfma_f32_16x16x32_bf16 v[174:177], v[178:181], v[182:185], v[174:177]
	ds_read_b128 v[182:185], v147 offset:43968
	s_waitcnt lgkmcnt(0)
	v_mfma_f32_16x16x32_bf16 v[50:53], v[178:181], v[182:185], v[50:53]
	ds_read2_b32 v[178:179], v149 offset1:16
	s_waitcnt vmcnt(7)
	v_lshlrev_b32_e32 v180, 16, v110
	v_and_b32_e32 v181, 0xffff0000, v110
	s_waitcnt lgkmcnt(0)
; #define LBAR() do { asm volatile("s_waitcnt lgkmcnt(0)" ::: "memory"); __builtin_amdgcn_s_barrier(); asm volatile("" ::: "memory"); } while (0)
; __device__ __forceinline__ unsigned pk2(float lo, float hi) { const f32v2 v = {lo, hi}; return __builtin_bit_cast(unsigned, __builtin_convertvector(v, bf16v2)); }
; __global__ void __launch_bounds__(NTHREADS, 2) fwd(Args args) {
;     ...
;                         for (int tp = 0; tp < 8; ++tp) { const int pp = 16 * tp + r16, e0 = 16 * wave + 4 * q4; const float bs = bsl[h * 128 + pp]; const u32x2 uu = ureg[tp];
;                             u32x2 o; o.x = pk2(bflo(uu.x) * (acc[tp][0] + bs), bfhi(uu.x) * (acc[tp][1] + bs)); o.y = pk2(bflo(uu.y) * (acc[tp][2] + bs), bfhi(uu.y) * (acc[tp][3] + bs));
;                             *(u32x2*)(ACAT + (size_t)(r0 + pp) * D + h * 128 + e0) = o; }
;                         LBAR();
;                     }
	v_pk_add_f32 v[150:151], v[178:179], v[150:151] op_sel_hi:[0,1]
	v_pk_mul_f32 v[150:151], v[150:151], v[180:181]
	v_pk_add_f32 v[152:153], v[178:179], v[152:153] op_sel_hi:[0,1]
	v_cvt_pk_bf16_f32 v110, v150, v151
	v_lshlrev_b32_e32 v150, 16, v111
	v_and_b32_e32 v151, 0xffff0000, v111
	v_pk_mul_f32 v[150:151], v[152:153], v[150:151]
	v_mov_b32_e32 v60, v179
	v_cvt_pk_bf16_f32 v111, v150, v151
	v_lshl_add_u64 v[150:151], v[78:79], 0, s[14:15]
	global_store_dwordx2 v[150:151], v[110:111], off
	s_waitcnt vmcnt(7)
	v_lshlrev_b32_e32 v110, 16, v108
	v_and_b32_e32 v111, 0xffff0000, v108
	v_pk_add_f32 v[150:151], v[60:61], v[154:155] op_sel_hi:[0,1]
	v_pk_mul_f32 v[110:111], v[150:151], v[110:111]
	v_pk_add_f32 v[150:151], v[60:61], v[156:157] op_sel_hi:[0,1]
	v_cvt_pk_bf16_f32 v108, v110, v111
	v_lshlrev_b32_e32 v110, 16, v109
	v_and_b32_e32 v111, 0xffff0000, v109
	v_pk_mul_f32 v[110:111], v[150:151], v[110:111]
	s_nop 0
	v_cvt_pk_bf16_f32 v109, v110, v111
	v_lshl_add_u64 v[110:111], v[76:77], 0, s[14:15]
	global_store_dwordx2 v[110:111], v[108:109], off
	ds_read2_b32 v[108:109], v149 offset0:32 offset1:48
	s_waitcnt vmcnt(7)
	v_lshlrev_b32_e32 v110, 16, v106
	v_and_b32_e32 v111, 0xffff0000, v106
	s_waitcnt lgkmcnt(0)
	v_pk_add_f32 v[150:151], v[108:109], v[158:159] op_sel_hi:[0,1]
	v_pk_mul_f32 v[110:111], v[150:151], v[110:111]
	v_pk_add_f32 v[150:151], v[108:109], v[160:161] op_sel_hi:[0,1]
	v_cvt_pk_bf16_f32 v106, v110, v111
	v_lshlrev_b32_e32 v110, 16, v107
	v_and_b32_e32 v111, 0xffff0000, v107
	v_pk_mul_f32 v[110:111], v[150:151], v[110:111]
	v_mov_b32_e32 v60, v109
	v_cvt_pk_bf16_f32 v107, v110, v111
	v_lshl_add_u64 v[110:111], v[74:75], 0, s[14:15]
	global_store_dwordx2 v[110:111], v[106:107], off
	s_waitcnt vmcnt(7)
	v_lshlrev_b32_e32 v106, 16, v104
	v_and_b32_e32 v107, 0xffff0000, v104
	v_pk_add_f32 v[108:109], v[60:61], v[162:163] op_sel_hi:[0,1]
	v_pk_mul_f32 v[106:107], v[108:109], v[106:107]
	v_pk_add_f32 v[108:109], v[60:61], v[164:165] op_sel_hi:[0,1]
	v_cvt_pk_bf16_f32 v104, v106, v107
	v_lshlrev_b32_e32 v106, 16, v105
	v_and_b32_e32 v107, 0xffff0000, v105
	v_pk_mul_f32 v[106:107], v[108:109], v[106:107]
	s_nop 0
	v_cvt_pk_bf16_f32 v105, v106, v107
	v_lshl_add_u64 v[106:107], v[72:73], 0, s[14:15]
	global_store_dwordx2 v[106:107], v[104:105], off
	ds_read2_b32 v[104:105], v149 offset0:64 offset1:80
	s_waitcnt vmcnt(7)
	v_lshlrev_b32_e32 v106, 16, v102
	v_and_b32_e32 v107, 0xffff0000, v102
	s_waitcnt lgkmcnt(0)
	v_pk_add_f32 v[108:109], v[104:105], v[166:167] op_sel_hi:[0,1]
	v_pk_mul_f32 v[106:107], v[108:109], v[106:107]
	v_pk_add_f32 v[108:109], v[104:105], v[168:169] op_sel_hi:[0,1]
	v_cvt_pk_bf16_f32 v102, v106, v107
	v_lshlrev_b32_e32 v106, 16, v103
	v_and_b32_e32 v107, 0xffff0000, v103
	v_pk_mul_f32 v[106:107], v[108:109], v[106:107]
	v_mov_b32_e32 v60, v105
	v_cvt_pk_bf16_f32 v103, v106, v107
	v_lshl_add_u64 v[106:107], v[70:71], 0, s[14:15]
	global_store_dwordx2 v[106:107], v[102:103], off
	s_waitcnt vmcnt(7)
	v_lshlrev_b32_e32 v102, 16, v100
	v_and_b32_e32 v103, 0xffff0000, v100
	v_pk_add_f32 v[104:105], v[60:61], v[170:171] op_sel_hi:[0,1]
	v_pk_mul_f32 v[102:103], v[104:105], v[102:103]
	v_pk_add_f32 v[104:105], v[60:61], v[172:173] op_sel_hi:[0,1]
	v_cvt_pk_bf16_f32 v100, v102, v103
	v_lshlrev_b32_e32 v102, 16, v101
	v_and_b32_e32 v103, 0xffff0000, v101
	v_pk_mul_f32 v[102:103], v[104:105], v[102:103]
	s_nop 0
	v_cvt_pk_bf16_f32 v101, v102, v103
	v_lshl_add_u64 v[102:103], v[68:69], 0, s[14:15]
	global_store_dwordx2 v[102:103], v[100:101], off
	ds_read2_b32 v[100:101], v149 offset0:96 offset1:112
	s_waitcnt vmcnt(7)
	v_lshlrev_b32_e32 v102, 16, v98
	v_and_b32_e32 v103, 0xffff0000, v98
	s_waitcnt lgkmcnt(0)
	v_pk_add_f32 v[104:105], v[100:101], v[174:175] op_sel_hi:[0,1]
	v_pk_mul_f32 v[102:103], v[104:105], v[102:103]
	v_pk_add_f32 v[104:105], v[100:101], v[176:177] op_sel_hi:[0,1]
	v_cvt_pk_bf16_f32 v98, v102, v103
	v_lshlrev_b32_e32 v102, 16, v99
	v_and_b32_e32 v103, 0xffff0000, v99
	v_pk_mul_f32 v[102:103], v[104:105], v[102:103]
	v_mov_b32_e32 v60, v101
	v_cvt_pk_bf16_f32 v99, v102, v103
	v_lshl_add_u64 v[102:103], v[56:57], 0, s[14:15]
	global_store_dwordx2 v[102:103], v[98:99], off
	s_waitcnt vmcnt(7)
	v_lshlrev_b32_e32 v98, 16, v96
	v_and_b32_e32 v99, 0xffff0000, v96
	v_pk_add_f32 v[50:51], v[60:61], v[50:51] op_sel_hi:[0,1]
	v_lshlrev_b32_e32 v96, 16, v97
	v_and_b32_e32 v97, 0xffff0000, v97
	v_pk_add_f32 v[52:53], v[60:61], v[52:53] op_sel_hi:[0,1]
	v_pk_mul_f32 v[50:51], v[50:51], v[98:99]
	v_pk_mul_f32 v[52:53], v[52:53], v[96:97]
	v_cvt_pk_bf16_f32 v50, v50, v51
	v_cvt_pk_bf16_f32 v51, v52, v53
	v_lshl_add_u64 v[52:53], v[54:55], 0, s[14:15]
	s_add_u32 s14, s14, 0x100
	global_store_dwordx2 v[52:53], v[50:51], off
	s_addc_u32 s15, s15, 0
	s_waitcnt lgkmcnt(0)
	s_barrier
	s_add_u32 s8, s8, 0x10000
	s_addc_u32 s9, s9, 0
	s_add_i32 s29, s29, 1
	s_addk_i32 s4, 0x200
	s_cmpk_eq_i32 s14, 0x800
	s_cbranch_scc1 .LBB0_441

; #define LAS __attribute__((address_space(3)))
; #define LDS_WAIT() asm volatile("s_waitcnt lgkmcnt(0)" ::: "memory")
; __device__ __forceinline__ void item8_load(const float* W, int N, int k0, int n0, int lane, f32x4 (&rg)[16]) {
; #pragma unroll
;     for (int i = 0; i < 16; ++i) rg[i] = __builtin_nontemporal_load((const f32x4*)(W + (size_t)(k0 + 8 * i + (lane >> 3)) * N + n0 + 4 * (lane & 7)));
; }
; __device__ __forceinline__ void item8_finish(int K, unsigned char* WT, int k0, int r0, LAS float* scr, int lane, const f32x4 (&rg)[16]) {
; #pragma unroll
;     for (int i = 0; i < 16; ++i) { LAS float* d = scr + (8 * i + (lane >> 3)) * 33 + 4 * (lane & 7); d[0] = rg[i].x; d[1] = rg[i].y; d[2] = rg[i].z; d[3] = rg[i].w; }
;     LDS_WAIT();
;     const int c = lane & 7;
; #pragma unroll
;     for (int j = 0; j < 4; ++j) { const int n = (lane >> 3) + 8 * j; const LAS float* sp = scr + (16 * c) * 33 + n; int w[4];
; #pragma unroll
;         for (int q = 0; q < 4; ++q) { w[q] = __builtin_amdgcn_cvt_pk_fp8_f32(sp[(4 * q) * 33] * 256.f, sp[(4 * q + 1) * 33] * 256.f, 0, false); w[q] = __builtin_amdgcn_cvt_pk_fp8_f32(sp[(4 * q + 2) * 33] * 256.f, sp[(4 * q + 3) * 33] * 256.f, w[q], true); }
;         u32x4 o; o.x = (unsigned)w[0]; o.y = (unsigned)w[1]; o.z = (unsigned)w[2]; o.w = (unsigned)w[3];
;         __builtin_nontemporal_store(o, (u32x4*)(WT + (size_t)(r0 + n) * K + k0 + 16 * c)); }
;     LDS_WAIT();
; }
.LBB0_464:
	v_writelane_b32 v247, s22, 0
	v_writelane_b32 v247, s23, 1
	v_writelane_b32 v247, s24, 2
	v_writelane_b32 v247, s25, 3
	v_writelane_b32 v247, s26, 4
	v_writelane_b32 v247, s27, 5
	v_writelane_b32 v247, s28, 6
	v_writelane_b32 v247, s29, 7
	v_writelane_b32 v247, s30, 8
	v_writelane_b32 v247, s31, 9
	v_writelane_b32 v247, s32, 10
	v_writelane_b32 v247, s33, 11
	s_mov_b64 exec, -1
	s_waitcnt vmcnt(0)
	v_readlane_b32 s3, v246, 21
	s_nop 3
	s_cmpk_gt_i32 s94, 0xbf
	s_cbranch_scc1 .Lfc4_conv
	s_sub_i32 s2, s94, 64
	s_lshl_b32 s2, s2, 3
	s_add_i32 s2, s2, s3
	s_add_i32 s2, s2, 14848
	s_mov_b32 s4, 20480
	s_movk_i32 s33, 1024
	s_branch .Lfc4_go
.Lfc4_conv:
	s_sub_i32 s2, s94, 192
	s_lshl_b32 s2, s2, 3
	s_add_i32 s2, s2, s3
	s_mov_b32 s4, 14848
	s_movk_i32 s33, 512
.Lfc4_go:
	s_cmp_lt_u32 s2, s4
	s_cbranch_scc0 .Lfc4_done
	v_mbcnt_lo_u32_b32 v208, -1, 0
	v_mbcnt_hi_u32_b32 v208, -1, v208
	v_lshrrev_b32_e32 v204, 3, v208
	v_and_b32_e32 v208, 7, v208
	v_lshlrev_b32_e32 v205, 4, v208
	v_lshlrev_b32_e32 v206, 13, v208
	v_lshl_add_u32 v206, v204, 4, v206
	v_readlane_b32 s14, v246, 8
	v_readlane_b32 s15, v246, 9
	s_nop 3
	s_sub_u32 s14, s14, 0x100
	s_subb_u32 s15, s15, 0
	s_load_dwordx2 s[18:19], s[14:15], 0xb8
	s_load_dwordx2 s[20:21], s[14:15], 0xc8
	s_mov_b32 s22, 0x43800000
	s_mov_b32 s23, 0x43800000
	s_mov_b32 s5, 0
	s_mov_b32 s3, s2
	s_waitcnt vmcnt(0) lgkmcnt(0)
	s_mov_b32 s26, 39424
	s_add_u32 s29, s2, s26
	s_cmp_lt_u32 s29, 0x10000
	s_cbranch_scc0 .Lfc4_sdp0
	s_lshr_b32 s30, s29, 11
	s_and_b32 s26, s29, 0x7ff
	s_lshr_b32 s31, s26, 7
	s_and_b32 s32, s26, 0x7f
	s_lshl_b32 s26, s30, 25
	s_lshl_b32 s27, s31, 21
	s_add_u32 s26, s26, s27
	s_lshl_b32 s27, s32, 7
	s_add_u32 s26, s26, s27
	s_add_u32 s6, s18, s26
	s_addc_u32 s7, s19, 0
	s_movk_i32 s24, 0x4000
	s_branch .Lfc4_scp0
.Lfc4_sdp0:
	s_sub_u32 s28, s29, 0x10000
	s_lshr_b32 s30, s28, 10
	s_and_b32 s26, s28, 0x3ff
	s_lshr_b32 s31, s26, 6
	s_and_b32 s32, s26, 0x3f
	s_lshl_b32 s26, s30, 24
	s_lshl_b32 s27, s31, 20
	s_add_u32 s26, s26, s27
	s_lshl_b32 s27, s32, 7
	s_add_u32 s26, s26, s27
	s_add_u32 s6, s20, s26
	s_addc_u32 s7, s21, 0
	s_movk_i32 s24, 0x2000
.Lfc4_scp0:
	s_lshl_b32 s25, s24, 4
	v_mad_u32_u24 v207, v204, s25, v205
	global_load_dwordx4 v[2:5], v207, s[6:7] nt
	s_add_u32 s6, s6, s24
	s_addc_u32 s7, s7, 0
	global_load_dwordx4 v[6:9], v207, s[6:7] nt
	s_add_u32 s6, s6, s24
	s_addc_u32 s7, s7, 0
	global_load_dwordx4 v[10:13], v207, s[6:7] nt
	s_add_u32 s6, s6, s24
	s_addc_u32 s7, s7, 0
	global_load_dwordx4 v[14:17], v207, s[6:7] nt
	s_add_u32 s6, s6, s24
	s_addc_u32 s7, s7, 0
	global_load_dwordx4 v[18:21], v207, s[6:7] nt
	s_add_u32 s6, s6, s24
	s_addc_u32 s7, s7, 0
	global_load_dwordx4 v[22:25], v207, s[6:7] nt
	s_add_u32 s6, s6, s24
	s_addc_u32 s7, s7, 0
	global_load_dwordx4 v[26:29], v207, s[6:7] nt
	s_add_u32 s6, s6, s24
	s_addc_u32 s7, s7, 0
	global_load_dwordx4 v[30:33], v207, s[6:7] nt
	s_add_u32 s6, s6, s24
	s_addc_u32 s7, s7, 0
	global_load_dwordx4 v[34:37], v207, s[6:7] nt
	s_add_u32 s6, s6, s24
	s_addc_u32 s7, s7, 0
	global_load_dwordx4 v[38:41], v207, s[6:7] nt
	s_add_u32 s6, s6, s24
	s_addc_u32 s7, s7, 0
	global_load_dwordx4 v[42:45], v207, s[6:7] nt
	s_add_u32 s6, s6, s24
	s_addc_u32 s7, s7, 0
	global_load_dwordx4 v[46:49], v207, s[6:7] nt
	s_add_u32 s6, s6, s24
	s_addc_u32 s7, s7, 0
	global_load_dwordx4 v[50:53], v207, s[6:7] nt
	s_add_u32 s6, s6, s24
	s_addc_u32 s7, s7, 0
	global_load_dwordx4 v[54:57], v207, s[6:7] nt
	s_add_u32 s6, s6, s24
	s_addc_u32 s7, s7, 0
	global_load_dwordx4 v[58:61], v207, s[6:7] nt
	s_add_u32 s6, s6, s24
	s_addc_u32 s7, s7, 0
	global_load_dwordx4 v[62:65], v207, s[6:7] nt
	s_add_u32 s2, s2, s33
	s_cmp_lt_u32 s2, s4
	s_cbranch_scc0 .Lfc4_body0
	s_mov_b32 s26, 39424
	s_add_u32 s29, s2, s26
	s_cmp_lt_u32 s29, 0x10000
	s_cbranch_scc0 .Lfc4_sdp1
	s_lshr_b32 s30, s29, 11
	s_and_b32 s26, s29, 0x7ff
	s_lshr_b32 s31, s26, 7
	s_and_b32 s32, s26, 0x7f
	s_lshl_b32 s26, s30, 25
	s_lshl_b32 s27, s31, 21
	s_add_u32 s26, s26, s27
	s_lshl_b32 s27, s32, 7
	s_add_u32 s26, s26, s27
	s_add_u32 s6, s18, s26
	s_addc_u32 s7, s19, 0
	s_movk_i32 s24, 0x4000
	s_branch .Lfc4_scp1

; __device__ __forceinline__ void item8_load(const float* W, int N, int k0, int n0, int lane, f32x4 (&rg)[16]) {
; #pragma unroll
;     for (int i = 0; i < 16; ++i) rg[i] = __builtin_nontemporal_load((const f32x4*)(W + (size_t)(k0 + 8 * i + (lane >> 3)) * N + n0 + 4 * (lane & 7)));
; }
.Lfc4_scp1:
	s_lshl_b32 s25, s24, 4
	v_mad_u32_u24 v207, v204, s25, v205
	global_load_dwordx4 v[66:69], v207, s[6:7] nt
	s_add_u32 s6, s6, s24
	s_addc_u32 s7, s7, 0
	global_load_dwordx4 v[70:73], v207, s[6:7] nt
	s_add_u32 s6, s6, s24
	s_addc_u32 s7, s7, 0
	global_load_dwordx4 v[74:77], v207, s[6:7] nt
	s_add_u32 s6, s6, s24
	s_addc_u32 s7, s7, 0
	global_load_dwordx4 v[78:81], v207, s[6:7] nt
	s_add_u32 s6, s6, s24
	s_addc_u32 s7, s7, 0
	global_load_dwordx4 v[82:85], v207, s[6:7] nt
	s_add_u32 s6, s6, s24
	s_addc_u32 s7, s7, 0
	global_load_dwordx4 v[86:89], v207, s[6:7] nt
	s_add_u32 s6, s6, s24
	s_addc_u32 s7, s7, 0
	global_load_dwordx4 v[90:93], v207, s[6:7] nt
	s_add_u32 s6, s6, s24
	s_addc_u32 s7, s7, 0
	global_load_dwordx4 v[94:97], v207, s[6:7] nt
	s_add_u32 s6, s6, s24
	s_addc_u32 s7, s7, 0
	global_load_dwordx4 v[98:101], v207, s[6:7] nt
	s_add_u32 s6, s6, s24
	s_addc_u32 s7, s7, 0
	global_load_dwordx4 v[102:105], v207, s[6:7] nt
	s_add_u32 s6, s6, s24
	s_addc_u32 s7, s7, 0
	global_load_dwordx4 v[106:109], v207, s[6:7] nt
	s_add_u32 s6, s6, s24
	s_addc_u32 s7, s7, 0
	global_load_dwordx4 v[110:113], v207, s[6:7] nt
	s_add_u32 s6, s6, s24
	s_addc_u32 s7, s7, 0
	global_load_dwordx4 v[114:117], v207, s[6:7] nt
	s_add_u32 s6, s6, s24
	s_addc_u32 s7, s7, 0
	global_load_dwordx4 v[118:121], v207, s[6:7] nt
	s_add_u32 s6, s6, s24
	s_addc_u32 s7, s7, 0
	global_load_dwordx4 v[122:125], v207, s[6:7] nt
	s_add_u32 s6, s6, s24
	s_addc_u32 s7, s7, 0
	global_load_dwordx4 v[126:129], v207, s[6:7] nt
.Lfc4_body0:
	s_add_u32 s2, s2, s33
	s_cmp_lt_u32 s2, s4
	s_cbranch_scc0 .Lfc4_nl0
	s_mov_b32 s26, 39424
	s_add_u32 s29, s2, s26
	s_cmp_lt_u32 s29, 0x10000
	s_cbranch_scc0 .Lfc4_sdb0
	s_lshr_b32 s30, s29, 11
	s_and_b32 s26, s29, 0x7ff
	s_lshr_b32 s31, s26, 7
	s_and_b32 s32, s26, 0x7f
	s_lshl_b32 s26, s30, 25
	s_lshl_b32 s27, s31, 21
	s_add_u32 s26, s26, s27
	s_lshl_b32 s27, s32, 7
	s_add_u32 s26, s26, s27
	s_add_u32 s6, s18, s26
	s_addc_u32 s7, s19, 0
	s_movk_i32 s24, 0x4000
	s_branch .Lfc4_scb0

; __device__ __forceinline__ void item8_load(const float* W, int N, int k0, int n0, int lane, f32x4 (&rg)[16]) {
; #pragma unroll
;     for (int i = 0; i < 16; ++i) rg[i] = __builtin_nontemporal_load((const f32x4*)(W + (size_t)(k0 + 8 * i + (lane >> 3)) * N + n0 + 4 * (lane & 7)));
; }
.Lfc4_scb0:
	s_lshl_b32 s25, s24, 4
	v_mad_u32_u24 v207, v204, s25, v205
	global_load_dwordx4 v[130:133], v207, s[6:7] nt
	s_add_u32 s6, s6, s24
	s_addc_u32 s7, s7, 0
	global_load_dwordx4 v[134:137], v207, s[6:7] nt
	s_add_u32 s6, s6, s24
	s_addc_u32 s7, s7, 0
	global_load_dwordx4 v[138:141], v207, s[6:7] nt
	s_add_u32 s6, s6, s24
	s_addc_u32 s7, s7, 0
	global_load_dwordx4 v[142:145], v207, s[6:7] nt
	s_add_u32 s6, s6, s24
	s_addc_u32 s7, s7, 0
	global_load_dwordx4 v[146:149], v207, s[6:7] nt
	s_add_u32 s6, s6, s24
	s_addc_u32 s7, s7, 0
	global_load_dwordx4 v[150:153], v207, s[6:7] nt
	s_add_u32 s6, s6, s24
	s_addc_u32 s7, s7, 0
	global_load_dwordx4 v[154:157], v207, s[6:7] nt
	s_add_u32 s6, s6, s24
	s_addc_u32 s7, s7, 0
	global_load_dwordx4 v[158:161], v207, s[6:7] nt
	s_add_u32 s6, s6, s24
	s_addc_u32 s7, s7, 0
	global_load_dwordx4 v[162:165], v207, s[6:7] nt
	s_add_u32 s6, s6, s24
	s_addc_u32 s7, s7, 0
	global_load_dwordx4 v[166:169], v207, s[6:7] nt
	s_add_u32 s6, s6, s24
	s_addc_u32 s7, s7, 0
	global_load_dwordx4 v[170:173], v207, s[6:7] nt
	s_add_u32 s6, s6, s24
	s_addc_u32 s7, s7, 0
	global_load_dwordx4 v[174:177], v207, s[6:7] nt
	s_add_u32 s6, s6, s24
	s_addc_u32 s7, s7, 0
	global_load_dwordx4 v[178:181], v207, s[6:7] nt
	s_add_u32 s6, s6, s24
	s_addc_u32 s7, s7, 0
	global_load_dwordx4 v[182:185], v207, s[6:7] nt
	s_add_u32 s6, s6, s24
	s_addc_u32 s7, s7, 0
	global_load_dwordx4 v[186:189], v207, s[6:7] nt
	s_add_u32 s6, s6, s24
	s_addc_u32 s7, s7, 0
	global_load_dwordx4 v[190:193], v207, s[6:7] nt
	s_mov_b32 s26, 39424
	s_add_u32 s29, s3, s26
	s_cmp_lt_u32 s29, 0x10000
	s_cbranch_scc0 .Lfc4_ddb0
	s_lshr_b32 s30, s29, 11
	s_and_b32 s26, s29, 0x7ff
	s_lshr_b32 s31, s26, 7
	s_and_b32 s32, s26, 0x7f
	s_and_b32 s26, s32, 63
	s_lshr_b32 s26, s26, 2
	s_lshl_b32 s26, s26, 8
	s_lshr_b32 s27, s32, 6
	s_lshl_b32 s27, s27, 7
	s_add_u32 s26, s26, s27
	s_and_b32 s27, s32, 3
	s_lshl_b32 s27, s27, 5
	s_add_u32 s26, s26, s27
	s_lshl_b32 s26, s26, 11
	s_lshl_b32 s27, s30, 23
	s_add_u32 s26, s26, s27
	s_lshl_b32 s27, s31, 7
	s_add_u32 s26, s26, s27
	s_add_u32 s26, s26, 0x4001000
	s_branch .Lfc4_dcb0
.Lfc4_ddb0:
	s_sub_u32 s28, s29, 0x10000
	s_lshr_b32 s30, s28, 10
	s_and_b32 s26, s28, 0x3ff
	s_lshr_b32 s31, s26, 6
	s_and_b32 s32, s26, 0x3f
	s_lshl_b32 s26, s30, 22
	s_lshl_b32 s27, s32, 16
	s_add_u32 s26, s26, s27
	s_lshl_b32 s27, s31, 7
	s_add_u32 s26, s26, s27
	s_add_u32 s26, s26, 0x24001000
.Lfc4_dcb0:
	s_add_u32 s8, s88, s26
	s_addc_u32 s9, s89, 0
	s_cmp_lt_u32 s5, 2
	s_cbranch_scc1 .Lfc4_w32_0
	s_waitcnt vmcnt(40)
	s_branch .Lfc4_cv0
.Lfc4_w32_0:
	s_waitcnt vmcnt(32)
	s_branch .Lfc4_cv0
.Lfc4_nl0:
	s_mov_b32 s26, 39424
	s_add_u32 s29, s3, s26
	s_cmp_lt_u32 s29, 0x10000
	s_cbranch_scc0 .Lfc4_ddn0
	s_lshr_b32 s30, s29, 11
	s_and_b32 s26, s29, 0x7ff
	s_lshr_b32 s31, s26, 7
	s_and_b32 s32, s26, 0x7f
	s_and_b32 s26, s32, 63
	s_lshr_b32 s26, s26, 2
	s_lshl_b32 s26, s26, 8
	s_lshr_b32 s27, s32, 6
	s_lshl_b32 s27, s27, 7
	s_add_u32 s26, s26, s27
	s_and_b32 s27, s32, 3
	s_lshl_b32 s27, s27, 5
	s_add_u32 s26, s26, s27
	s_lshl_b32 s26, s26, 11
	s_lshl_b32 s27, s30, 23
	s_add_u32 s26, s26, s27
	s_lshl_b32 s27, s31, 7
	s_add_u32 s26, s26, s27
	s_add_u32 s26, s26, 0x4001000
	s_branch .Lfc4_dcn0

; #define LAS __attribute__((address_space(3)))
; #define LDS_WAIT() asm volatile("s_waitcnt lgkmcnt(0)" ::: "memory")
; __device__ __forceinline__ void item8_finish(int K, unsigned char* WT, int k0, int r0, LAS float* scr, int lane, const f32x4 (&rg)[16]) {
; #pragma unroll
;     for (int i = 0; i < 16; ++i) { LAS float* d = scr + (8 * i + (lane >> 3)) * 33 + 4 * (lane & 7); d[0] = rg[i].x; d[1] = rg[i].y; d[2] = rg[i].z; d[3] = rg[i].w; }
;     LDS_WAIT();
;     const int c = lane & 7;
; #pragma unroll
;     for (int j = 0; j < 4; ++j) { const int n = (lane >> 3) + 8 * j; const LAS float* sp = scr + (16 * c) * 33 + n; int w[4];
; #pragma unroll
;         for (int q = 0; q < 4; ++q) { w[q] = __builtin_amdgcn_cvt_pk_fp8_f32(sp[(4 * q) * 33] * 256.f, sp[(4 * q + 1) * 33] * 256.f, 0, false); w[q] = __builtin_amdgcn_cvt_pk_fp8_f32(sp[(4 * q + 2) * 33] * 256.f, sp[(4 * q + 3) * 33] * 256.f, w[q], true); }
;         u32x4 o; o.x = (unsigned)w[0]; o.y = (unsigned)w[1]; o.z = (unsigned)w[2]; o.w = (unsigned)w[3];
;         __builtin_nontemporal_store(o, (u32x4*)(WT + (size_t)(r0 + n) * K + k0 + 16 * c)); }
;     LDS_WAIT();
; }
.Lfc4_dcn0:
	s_add_u32 s8, s88, s26
	s_addc_u32 s9, s89, 0
	s_waitcnt vmcnt(0)
.Lfc4_cv0:
	v_pk_mul_f32 v[2:3], v[2:3], s[22:23]
	v_pk_mul_f32 v[4:5], v[4:5], s[22:23]
	v_pk_mul_f32 v[6:7], v[6:7], s[22:23]
	v_pk_mul_f32 v[8:9], v[8:9], s[22:23]
	v_pk_mul_f32 v[10:11], v[10:11], s[22:23]
	v_pk_mul_f32 v[12:13], v[12:13], s[22:23]
	v_pk_mul_f32 v[14:15], v[14:15], s[22:23]
	v_pk_mul_f32 v[16:17], v[16:17], s[22:23]
	v_pk_mul_f32 v[18:19], v[18:19], s[22:23]
	v_pk_mul_f32 v[20:21], v[20:21], s[22:23]
	v_pk_mul_f32 v[22:23], v[22:23], s[22:23]
	v_pk_mul_f32 v[24:25], v[24:25], s[22:23]
	v_pk_mul_f32 v[26:27], v[26:27], s[22:23]
	v_pk_mul_f32 v[28:29], v[28:29], s[22:23]
	v_pk_mul_f32 v[30:31], v[30:31], s[22:23]
	v_pk_mul_f32 v[32:33], v[32:33], s[22:23]
	v_pk_mul_f32 v[34:35], v[34:35], s[22:23]
	v_pk_mul_f32 v[36:37], v[36:37], s[22:23]
	v_pk_mul_f32 v[38:39], v[38:39], s[22:23]
	v_pk_mul_f32 v[40:41], v[40:41], s[22:23]
	v_pk_mul_f32 v[42:43], v[42:43], s[22:23]
	v_pk_mul_f32 v[44:45], v[44:45], s[22:23]
	v_pk_mul_f32 v[46:47], v[46:47], s[22:23]
	v_pk_mul_f32 v[48:49], v[48:49], s[22:23]
	v_pk_mul_f32 v[50:51], v[50:51], s[22:23]
	v_pk_mul_f32 v[52:53], v[52:53], s[22:23]
	v_pk_mul_f32 v[54:55], v[54:55], s[22:23]
	v_pk_mul_f32 v[56:57], v[56:57], s[22:23]
	v_pk_mul_f32 v[58:59], v[58:59], s[22:23]
	v_pk_mul_f32 v[60:61], v[60:61], s[22:23]
	v_pk_mul_f32 v[62:63], v[62:63], s[22:23]
	v_pk_mul_f32 v[64:65], v[64:65], s[22:23]
	v_cvt_pk_fp8_f32 v196, v2, v6
	v_cvt_pk_fp8_f32 v197, v18, v22
	v_cvt_pk_fp8_f32 v198, v34, v38
	v_cvt_pk_fp8_f32 v199, v50, v54
	v_cvt_pk_fp8_f32 v196, v10, v14 op_sel:[0,0,1]
	v_cvt_pk_fp8_f32 v197, v26, v30 op_sel:[0,0,1]
	v_cvt_pk_fp8_f32 v198, v42, v46 op_sel:[0,0,1]
	v_cvt_pk_fp8_f32 v199, v58, v62 op_sel:[0,0,1]
	s_nop 0
	global_store_dwordx4 v206, v[196:199], s[8:9] offset:-4096 nt
	v_cvt_pk_fp8_f32 v200, v3, v7
	v_cvt_pk_fp8_f32 v201, v19, v23
	v_cvt_pk_fp8_f32 v202, v35, v39
	v_cvt_pk_fp8_f32 v203, v51, v55
	v_cvt_pk_fp8_f32 v200, v11, v15 op_sel:[0,0,1]
	v_cvt_pk_fp8_f32 v201, v27, v31 op_sel:[0,0,1]
	v_cvt_pk_fp8_f32 v202, v43, v47 op_sel:[0,0,1]
	v_cvt_pk_fp8_f32 v203, v59, v63 op_sel:[0,0,1]
	s_nop 0
	global_store_dwordx4 v206, v[200:203], s[8:9] offset:-2048 nt
	v_cvt_pk_fp8_f32 v196, v4, v8
	v_cvt_pk_fp8_f32 v197, v20, v24
	v_cvt_pk_fp8_f32 v198, v36, v40
	v_cvt_pk_fp8_f32 v199, v52, v56
	v_cvt_pk_fp8_f32 v196, v12, v16 op_sel:[0,0,1]
	v_cvt_pk_fp8_f32 v197, v28, v32 op_sel:[0,0,1]
	v_cvt_pk_fp8_f32 v198, v44, v48 op_sel:[0,0,1]
	v_cvt_pk_fp8_f32 v199, v60, v64 op_sel:[0,0,1]
	s_nop 0
	global_store_dwordx4 v206, v[196:199], s[8:9] offset:0 nt
	v_cvt_pk_fp8_f32 v200, v5, v9
	v_cvt_pk_fp8_f32 v201, v21, v25
	v_cvt_pk_fp8_f32 v202, v37, v41
	v_cvt_pk_fp8_f32 v203, v53, v57
	v_cvt_pk_fp8_f32 v200, v13, v17 op_sel:[0,0,1]
	v_cvt_pk_fp8_f32 v201, v29, v33 op_sel:[0,0,1]
	v_cvt_pk_fp8_f32 v202, v45, v49 op_sel:[0,0,1]
	v_cvt_pk_fp8_f32 v203, v61, v65 op_sel:[0,0,1]
	s_nop 0
	global_store_dwordx4 v206, v[200:203], s[8:9] offset:2048 nt
	s_add_u32 s3, s3, s33
	s_add_u32 s5, s5, 1
	s_cmp_lt_u32 s3, s4
	s_cbranch_scc0 .Lfc4_fin

; __device__ __forceinline__ void item8_load(const float* W, int N, int k0, int n0, int lane, f32x4 (&rg)[16]) {
; #pragma unroll
;     for (int i = 0; i < 16; ++i) rg[i] = __builtin_nontemporal_load((const f32x4*)(W + (size_t)(k0 + 8 * i + (lane >> 3)) * N + n0 + 4 * (lane & 7)));
; }
.Lfc4_scb1:
	s_lshl_b32 s25, s24, 4
	v_mad_u32_u24 v207, v204, s25, v205
	global_load_dwordx4 v[2:5], v207, s[6:7] nt
	s_add_u32 s6, s6, s24
	s_addc_u32 s7, s7, 0
	global_load_dwordx4 v[6:9], v207, s[6:7] nt
	s_add_u32 s6, s6, s24
	s_addc_u32 s7, s7, 0
	global_load_dwordx4 v[10:13], v207, s[6:7] nt
	s_add_u32 s6, s6, s24
	s_addc_u32 s7, s7, 0
	global_load_dwordx4 v[14:17], v207, s[6:7] nt
	s_add_u32 s6, s6, s24
	s_addc_u32 s7, s7, 0
	global_load_dwordx4 v[18:21], v207, s[6:7] nt
	s_add_u32 s6, s6, s24
	s_addc_u32 s7, s7, 0
	global_load_dwordx4 v[22:25], v207, s[6:7] nt
	s_add_u32 s6, s6, s24
	s_addc_u32 s7, s7, 0
	global_load_dwordx4 v[26:29], v207, s[6:7] nt
	s_add_u32 s6, s6, s24
	s_addc_u32 s7, s7, 0
	global_load_dwordx4 v[30:33], v207, s[6:7] nt
	s_add_u32 s6, s6, s24
	s_addc_u32 s7, s7, 0
	global_load_dwordx4 v[34:37], v207, s[6:7] nt
	s_add_u32 s6, s6, s24
	s_addc_u32 s7, s7, 0
	global_load_dwordx4 v[38:41], v207, s[6:7] nt
	s_add_u32 s6, s6, s24
	s_addc_u32 s7, s7, 0
	global_load_dwordx4 v[42:45], v207, s[6:7] nt
	s_add_u32 s6, s6, s24
	s_addc_u32 s7, s7, 0
	global_load_dwordx4 v[46:49], v207, s[6:7] nt
	s_add_u32 s6, s6, s24
	s_addc_u32 s7, s7, 0
	global_load_dwordx4 v[50:53], v207, s[6:7] nt
	s_add_u32 s6, s6, s24
	s_addc_u32 s7, s7, 0
	global_load_dwordx4 v[54:57], v207, s[6:7] nt
	s_add_u32 s6, s6, s24
	s_addc_u32 s7, s7, 0
	global_load_dwordx4 v[58:61], v207, s[6:7] nt
	s_add_u32 s6, s6, s24
	s_addc_u32 s7, s7, 0
	global_load_dwordx4 v[62:65], v207, s[6:7] nt
	s_mov_b32 s26, 39424
	s_add_u32 s29, s3, s26
	s_cmp_lt_u32 s29, 0x10000
	s_cbranch_scc0 .Lfc4_ddb1
	s_lshr_b32 s30, s29, 11
	s_and_b32 s26, s29, 0x7ff
	s_lshr_b32 s31, s26, 7
	s_and_b32 s32, s26, 0x7f
	s_and_b32 s26, s32, 63
	s_lshr_b32 s26, s26, 2
	s_lshl_b32 s26, s26, 8
	s_lshr_b32 s27, s32, 6
	s_lshl_b32 s27, s27, 7
	s_add_u32 s26, s26, s27
	s_and_b32 s27, s32, 3
	s_lshl_b32 s27, s27, 5
	s_add_u32 s26, s26, s27
	s_lshl_b32 s26, s26, 11
	s_lshl_b32 s27, s30, 23
	s_add_u32 s26, s26, s27
	s_lshl_b32 s27, s31, 7
	s_add_u32 s26, s26, s27
	s_add_u32 s26, s26, 0x4001000
	s_branch .Lfc4_dcb1

; #define LAS __attribute__((address_space(3)))
; #define LDS_WAIT() asm volatile("s_waitcnt lgkmcnt(0)" ::: "memory")
; __device__ __forceinline__ void item8_finish(int K, unsigned char* WT, int k0, int r0, LAS float* scr, int lane, const f32x4 (&rg)[16]) {
; #pragma unroll
;     for (int i = 0; i < 16; ++i) { LAS float* d = scr + (8 * i + (lane >> 3)) * 33 + 4 * (lane & 7); d[0] = rg[i].x; d[1] = rg[i].y; d[2] = rg[i].z; d[3] = rg[i].w; }
;     LDS_WAIT();
;     const int c = lane & 7;
; #pragma unroll
;     for (int j = 0; j < 4; ++j) { const int n = (lane >> 3) + 8 * j; const LAS float* sp = scr + (16 * c) * 33 + n; int w[4];
; #pragma unroll
;         for (int q = 0; q < 4; ++q) { w[q] = __builtin_amdgcn_cvt_pk_fp8_f32(sp[(4 * q) * 33] * 256.f, sp[(4 * q + 1) * 33] * 256.f, 0, false); w[q] = __builtin_amdgcn_cvt_pk_fp8_f32(sp[(4 * q + 2) * 33] * 256.f, sp[(4 * q + 3) * 33] * 256.f, w[q], true); }
;         u32x4 o; o.x = (unsigned)w[0]; o.y = (unsigned)w[1]; o.z = (unsigned)w[2]; o.w = (unsigned)w[3];
;         __builtin_nontemporal_store(o, (u32x4*)(WT + (size_t)(r0 + n) * K + k0 + 16 * c)); }
;     LDS_WAIT();
; }
.Lfc4_cv1:
	v_pk_mul_f32 v[66:67], v[66:67], s[22:23]
	v_pk_mul_f32 v[68:69], v[68:69], s[22:23]
	v_pk_mul_f32 v[70:71], v[70:71], s[22:23]
	v_pk_mul_f32 v[72:73], v[72:73], s[22:23]
	v_pk_mul_f32 v[74:75], v[74:75], s[22:23]
	v_pk_mul_f32 v[76:77], v[76:77], s[22:23]
	v_pk_mul_f32 v[78:79], v[78:79], s[22:23]
	v_pk_mul_f32 v[80:81], v[80:81], s[22:23]
	v_pk_mul_f32 v[82:83], v[82:83], s[22:23]
	v_pk_mul_f32 v[84:85], v[84:85], s[22:23]
	v_pk_mul_f32 v[86:87], v[86:87], s[22:23]
	v_pk_mul_f32 v[88:89], v[88:89], s[22:23]
	v_pk_mul_f32 v[90:91], v[90:91], s[22:23]
	v_pk_mul_f32 v[92:93], v[92:93], s[22:23]
	v_pk_mul_f32 v[94:95], v[94:95], s[22:23]
	v_pk_mul_f32 v[96:97], v[96:97], s[22:23]
	v_pk_mul_f32 v[98:99], v[98:99], s[22:23]
	v_pk_mul_f32 v[100:101], v[100:101], s[22:23]
	v_pk_mul_f32 v[102:103], v[102:103], s[22:23]
	v_pk_mul_f32 v[104:105], v[104:105], s[22:23]
	v_pk_mul_f32 v[106:107], v[106:107], s[22:23]
	v_pk_mul_f32 v[108:109], v[108:109], s[22:23]
	v_pk_mul_f32 v[110:111], v[110:111], s[22:23]
	v_pk_mul_f32 v[112:113], v[112:113], s[22:23]
	v_pk_mul_f32 v[114:115], v[114:115], s[22:23]
	v_pk_mul_f32 v[116:117], v[116:117], s[22:23]
	v_pk_mul_f32 v[118:119], v[118:119], s[22:23]
	v_pk_mul_f32 v[120:121], v[120:121], s[22:23]
	v_pk_mul_f32 v[122:123], v[122:123], s[22:23]
	v_pk_mul_f32 v[124:125], v[124:125], s[22:23]
	v_pk_mul_f32 v[126:127], v[126:127], s[22:23]
	v_pk_mul_f32 v[128:129], v[128:129], s[22:23]
	v_cvt_pk_fp8_f32 v196, v66, v70
	v_cvt_pk_fp8_f32 v197, v82, v86
	v_cvt_pk_fp8_f32 v198, v98, v102
	v_cvt_pk_fp8_f32 v199, v114, v118
	v_cvt_pk_fp8_f32 v196, v74, v78 op_sel:[0,0,1]
	v_cvt_pk_fp8_f32 v197, v90, v94 op_sel:[0,0,1]
	v_cvt_pk_fp8_f32 v198, v106, v110 op_sel:[0,0,1]
	v_cvt_pk_fp8_f32 v199, v122, v126 op_sel:[0,0,1]
	s_nop 0
	global_store_dwordx4 v206, v[196:199], s[8:9] offset:-4096 nt
	v_cvt_pk_fp8_f32 v200, v67, v71
	v_cvt_pk_fp8_f32 v201, v83, v87
	v_cvt_pk_fp8_f32 v202, v99, v103
	v_cvt_pk_fp8_f32 v203, v115, v119
	v_cvt_pk_fp8_f32 v200, v75, v79 op_sel:[0,0,1]
	v_cvt_pk_fp8_f32 v201, v91, v95 op_sel:[0,0,1]
	v_cvt_pk_fp8_f32 v202, v107, v111 op_sel:[0,0,1]
	v_cvt_pk_fp8_f32 v203, v123, v127 op_sel:[0,0,1]
	s_nop 0
	global_store_dwordx4 v206, v[200:203], s[8:9] offset:-2048 nt
	v_cvt_pk_fp8_f32 v196, v68, v72
	v_cvt_pk_fp8_f32 v197, v84, v88
	v_cvt_pk_fp8_f32 v198, v100, v104
	v_cvt_pk_fp8_f32 v199, v116, v120
	v_cvt_pk_fp8_f32 v196, v76, v80 op_sel:[0,0,1]
	v_cvt_pk_fp8_f32 v197, v92, v96 op_sel:[0,0,1]
	v_cvt_pk_fp8_f32 v198, v108, v112 op_sel:[0,0,1]
	v_cvt_pk_fp8_f32 v199, v124, v128 op_sel:[0,0,1]
	s_nop 0
	global_store_dwordx4 v206, v[196:199], s[8:9] offset:0 nt
	v_cvt_pk_fp8_f32 v200, v69, v73
	v_cvt_pk_fp8_f32 v201, v85, v89
	v_cvt_pk_fp8_f32 v202, v101, v105
	v_cvt_pk_fp8_f32 v203, v117, v121
	v_cvt_pk_fp8_f32 v200, v77, v81 op_sel:[0,0,1]
	v_cvt_pk_fp8_f32 v201, v93, v97 op_sel:[0,0,1]
	v_cvt_pk_fp8_f32 v202, v109, v113 op_sel:[0,0,1]
	v_cvt_pk_fp8_f32 v203, v125, v129 op_sel:[0,0,1]
	s_nop 0
	global_store_dwordx4 v206, v[200:203], s[8:9] offset:2048 nt
	s_add_u32 s3, s3, s33
	s_add_u32 s5, s5, 1
	s_cmp_lt_u32 s3, s4
	s_cbranch_scc0 .Lfc4_fin

; __device__ __forceinline__ void item8_load(const float* W, int N, int k0, int n0, int lane, f32x4 (&rg)[16]) {
; #pragma unroll
;     for (int i = 0; i < 16; ++i) rg[i] = __builtin_nontemporal_load((const f32x4*)(W + (size_t)(k0 + 8 * i + (lane >> 3)) * N + n0 + 4 * (lane & 7)));
; }
.Lfc4_scb2:
	s_lshl_b32 s25, s24, 4
	v_mad_u32_u24 v207, v204, s25, v205
	global_load_dwordx4 v[66:69], v207, s[6:7] nt
	s_add_u32 s6, s6, s24
	s_addc_u32 s7, s7, 0
	global_load_dwordx4 v[70:73], v207, s[6:7] nt
	s_add_u32 s6, s6, s24
	s_addc_u32 s7, s7, 0
	global_load_dwordx4 v[74:77], v207, s[6:7] nt
	s_add_u32 s6, s6, s24
	s_addc_u32 s7, s7, 0
	global_load_dwordx4 v[78:81], v207, s[6:7] nt
	s_add_u32 s6, s6, s24
	s_addc_u32 s7, s7, 0
	global_load_dwordx4 v[82:85], v207, s[6:7] nt
	s_add_u32 s6, s6, s24
	s_addc_u32 s7, s7, 0
	global_load_dwordx4 v[86:89], v207, s[6:7] nt
	s_add_u32 s6, s6, s24
	s_addc_u32 s7, s7, 0
	global_load_dwordx4 v[90:93], v207, s[6:7] nt
	s_add_u32 s6, s6, s24
	s_addc_u32 s7, s7, 0
	global_load_dwordx4 v[94:97], v207, s[6:7] nt
	s_add_u32 s6, s6, s24
	s_addc_u32 s7, s7, 0
	global_load_dwordx4 v[98:101], v207, s[6:7] nt
	s_add_u32 s6, s6, s24
	s_addc_u32 s7, s7, 0
	global_load_dwordx4 v[102:105], v207, s[6:7] nt
	s_add_u32 s6, s6, s24
	s_addc_u32 s7, s7, 0
	global_load_dwordx4 v[106:109], v207, s[6:7] nt
	s_add_u32 s6, s6, s24
	s_addc_u32 s7, s7, 0
	global_load_dwordx4 v[110:113], v207, s[6:7] nt
	s_add_u32 s6, s6, s24
	s_addc_u32 s7, s7, 0
	global_load_dwordx4 v[114:117], v207, s[6:7] nt
	s_add_u32 s6, s6, s24
	s_addc_u32 s7, s7, 0
	global_load_dwordx4 v[118:121], v207, s[6:7] nt
	s_add_u32 s6, s6, s24
	s_addc_u32 s7, s7, 0
	global_load_dwordx4 v[122:125], v207, s[6:7] nt
	s_add_u32 s6, s6, s24
	s_addc_u32 s7, s7, 0
	global_load_dwordx4 v[126:129], v207, s[6:7] nt
	s_mov_b32 s26, 39424
	s_add_u32 s29, s3, s26
	s_cmp_lt_u32 s29, 0x10000
	s_cbranch_scc0 .Lfc4_ddb2
	s_lshr_b32 s30, s29, 11
	s_and_b32 s26, s29, 0x7ff
	s_lshr_b32 s31, s26, 7
	s_and_b32 s32, s26, 0x7f
	s_and_b32 s26, s32, 63
	s_lshr_b32 s26, s26, 2
	s_lshl_b32 s26, s26, 8
	s_lshr_b32 s27, s32, 6
	s_lshl_b32 s27, s27, 7
	s_add_u32 s26, s26, s27
	s_and_b32 s27, s32, 3
	s_lshl_b32 s27, s27, 5
	s_add_u32 s26, s26, s27
	s_lshl_b32 s26, s26, 11
	s_lshl_b32 s27, s30, 23
	s_add_u32 s26, s26, s27
	s_lshl_b32 s27, s31, 7
	s_add_u32 s26, s26, s27
	s_add_u32 s26, s26, 0x4001000
	s_branch .Lfc4_dcb2

; #define LAS __attribute__((address_space(3)))
; #define LDS_WAIT() asm volatile("s_waitcnt lgkmcnt(0)" ::: "memory")
; __device__ __forceinline__ void item8_finish(int K, unsigned char* WT, int k0, int r0, LAS float* scr, int lane, const f32x4 (&rg)[16]) {
; #pragma unroll
;     for (int i = 0; i < 16; ++i) { LAS float* d = scr + (8 * i + (lane >> 3)) * 33 + 4 * (lane & 7); d[0] = rg[i].x; d[1] = rg[i].y; d[2] = rg[i].z; d[3] = rg[i].w; }
;     LDS_WAIT();
;     const int c = lane & 7;
; #pragma unroll
;     for (int j = 0; j < 4; ++j) { const int n = (lane >> 3) + 8 * j; const LAS float* sp = scr + (16 * c) * 33 + n; int w[4];
; #pragma unroll
;         for (int q = 0; q < 4; ++q) { w[q] = __builtin_amdgcn_cvt_pk_fp8_f32(sp[(4 * q) * 33] * 256.f, sp[(4 * q + 1) * 33] * 256.f, 0, false); w[q] = __builtin_amdgcn_cvt_pk_fp8_f32(sp[(4 * q + 2) * 33] * 256.f, sp[(4 * q + 3) * 33] * 256.f, w[q], true); }
;         u32x4 o; o.x = (unsigned)w[0]; o.y = (unsigned)w[1]; o.z = (unsigned)w[2]; o.w = (unsigned)w[3];
;         __builtin_nontemporal_store(o, (u32x4*)(WT + (size_t)(r0 + n) * K + k0 + 16 * c)); }
;     LDS_WAIT();
; }
.Lfc4_cv2:
	v_pk_mul_f32 v[130:131], v[130:131], s[22:23]
	v_pk_mul_f32 v[132:133], v[132:133], s[22:23]
	v_pk_mul_f32 v[134:135], v[134:135], s[22:23]
	v_pk_mul_f32 v[136:137], v[136:137], s[22:23]
	v_pk_mul_f32 v[138:139], v[138:139], s[22:23]
	v_pk_mul_f32 v[140:141], v[140:141], s[22:23]
	v_pk_mul_f32 v[142:143], v[142:143], s[22:23]
	v_pk_mul_f32 v[144:145], v[144:145], s[22:23]
	v_pk_mul_f32 v[146:147], v[146:147], s[22:23]
	v_pk_mul_f32 v[148:149], v[148:149], s[22:23]
	v_pk_mul_f32 v[150:151], v[150:151], s[22:23]
	v_pk_mul_f32 v[152:153], v[152:153], s[22:23]
	v_pk_mul_f32 v[154:155], v[154:155], s[22:23]
	v_pk_mul_f32 v[156:157], v[156:157], s[22:23]
	v_pk_mul_f32 v[158:159], v[158:159], s[22:23]
	v_pk_mul_f32 v[160:161], v[160:161], s[22:23]
	v_pk_mul_f32 v[162:163], v[162:163], s[22:23]
	v_pk_mul_f32 v[164:165], v[164:165], s[22:23]
	v_pk_mul_f32 v[166:167], v[166:167], s[22:23]
	v_pk_mul_f32 v[168:169], v[168:169], s[22:23]
	v_pk_mul_f32 v[170:171], v[170:171], s[22:23]
	v_pk_mul_f32 v[172:173], v[172:173], s[22:23]
	v_pk_mul_f32 v[174:175], v[174:175], s[22:23]
	v_pk_mul_f32 v[176:177], v[176:177], s[22:23]
	v_pk_mul_f32 v[178:179], v[178:179], s[22:23]
	v_pk_mul_f32 v[180:181], v[180:181], s[22:23]
	v_pk_mul_f32 v[182:183], v[182:183], s[22:23]
	v_pk_mul_f32 v[184:185], v[184:185], s[22:23]
	v_pk_mul_f32 v[186:187], v[186:187], s[22:23]
	v_pk_mul_f32 v[188:189], v[188:189], s[22:23]
	v_pk_mul_f32 v[190:191], v[190:191], s[22:23]
	v_pk_mul_f32 v[192:193], v[192:193], s[22:23]
	v_cvt_pk_fp8_f32 v196, v130, v134
	v_cvt_pk_fp8_f32 v197, v146, v150
	v_cvt_pk_fp8_f32 v198, v162, v166
	v_cvt_pk_fp8_f32 v199, v178, v182
	v_cvt_pk_fp8_f32 v196, v138, v142 op_sel:[0,0,1]
	v_cvt_pk_fp8_f32 v197, v154, v158 op_sel:[0,0,1]
	v_cvt_pk_fp8_f32 v198, v170, v174 op_sel:[0,0,1]
	v_cvt_pk_fp8_f32 v199, v186, v190 op_sel:[0,0,1]
	s_nop 0
	global_store_dwordx4 v206, v[196:199], s[8:9] offset:-4096 nt
	v_cvt_pk_fp8_f32 v200, v131, v135
	v_cvt_pk_fp8_f32 v201, v147, v151
	v_cvt_pk_fp8_f32 v202, v163, v167
	v_cvt_pk_fp8_f32 v203, v179, v183
	v_cvt_pk_fp8_f32 v200, v139, v143 op_sel:[0,0,1]
	v_cvt_pk_fp8_f32 v201, v155, v159 op_sel:[0,0,1]
	v_cvt_pk_fp8_f32 v202, v171, v175 op_sel:[0,0,1]
	v_cvt_pk_fp8_f32 v203, v187, v191 op_sel:[0,0,1]
	s_nop 0
	global_store_dwordx4 v206, v[200:203], s[8:9] offset:-2048 nt
	v_cvt_pk_fp8_f32 v196, v132, v136
	v_cvt_pk_fp8_f32 v197, v148, v152
	v_cvt_pk_fp8_f32 v198, v164, v168
	v_cvt_pk_fp8_f32 v199, v180, v184
	v_cvt_pk_fp8_f32 v196, v140, v144 op_sel:[0,0,1]
	v_cvt_pk_fp8_f32 v197, v156, v160 op_sel:[0,0,1]
	v_cvt_pk_fp8_f32 v198, v172, v176 op_sel:[0,0,1]
	v_cvt_pk_fp8_f32 v199, v188, v192 op_sel:[0,0,1]
	s_nop 0
	global_store_dwordx4 v206, v[196:199], s[8:9] offset:0 nt
	v_cvt_pk_fp8_f32 v200, v133, v137
	v_cvt_pk_fp8_f32 v201, v149, v153
	v_cvt_pk_fp8_f32 v202, v165, v169
	v_cvt_pk_fp8_f32 v203, v181, v185
	v_cvt_pk_fp8_f32 v200, v141, v145 op_sel:[0,0,1]
	v_cvt_pk_fp8_f32 v201, v157, v161 op_sel:[0,0,1]
	v_cvt_pk_fp8_f32 v202, v173, v177 op_sel:[0,0,1]
	v_cvt_pk_fp8_f32 v203, v189, v193 op_sel:[0,0,1]
	s_nop 0
	global_store_dwordx4 v206, v[200:203], s[8:9] offset:2048 nt
	s_add_u32 s3, s3, s33
	s_add_u32 s5, s5, 1
	s_cmp_lt_u32 s3, s4
	s_cbranch_scc1 .Lfc4_body0

; #define MOE_RANGE(first_, end_, stride_) do { f32x4 rgA_[16], rgB_[16]; int ia_ = (first_); if (ia_ < (end_)) MOE_LOAD(ia_, rgA_); \
;         while (ia_ < (end_)) { const int ib_ = ia_ + (stride_); if (ib_ < (end_)) MOE_LOAD(ib_, rgB_); MOE_FIN(ia_, rgA_); if (ib_ >= (end_)) break; \
;             ia_ = ib_ + (stride_); if (ia_ < (end_)) MOE_LOAD(ia_, rgA_); MOE_FIN(ib_, rgB_); } } while (0)
; __global__ void __launch_bounds__(NTHREADS, 2) fwd(Args args) {
;     ...
;             if (bid >= 64 + NCMB && wave < 6) MOE_RANGE(CV_P0 + CV2 + CV2X + CV3 + (bid - 64 - NCMB) * 6 + wave, CV_P0 + CV2 + CV2X + CV3 + CV4 - CV4P0, (G - 64 - NCMB) * 6);
.Lfc4_done:
	v_readlane_b32 s22, v247, 0
	v_readlane_b32 s23, v247, 1
	v_readlane_b32 s24, v247, 2
	v_readlane_b32 s25, v247, 3
	v_readlane_b32 s26, v247, 4
	v_readlane_b32 s27, v247, 5
	v_readlane_b32 s28, v247, 6
	v_readlane_b32 s29, v247, 7
	v_readlane_b32 s30, v247, 8
	v_readlane_b32 s31, v247, 9
	v_readlane_b32 s32, v247, 10
	v_readlane_b32 s33, v247, 11
	s_nop 3

; __global__ void __launch_bounds__(NTHREADS, 2) fwd(Args args) {
	.amdhsa_kernel _Z3fwd4Args
		.amdhsa_group_segment_fixed_size 0
		.amdhsa_private_segment_fixed_size 0
		.amdhsa_kernarg_size 512
		.amdhsa_user_sgpr_count 2
		.amdhsa_user_sgpr_dispatch_ptr 0
		.amdhsa_user_sgpr_queue_ptr 0
		.amdhsa_user_sgpr_kernarg_segment_ptr 1
		.amdhsa_user_sgpr_dispatch_id 0
		.amdhsa_user_sgpr_kernarg_preload_length 0
		.amdhsa_user_sgpr_kernarg_preload_offset 0
		.amdhsa_user_sgpr_private_segment_size 0
		.amdhsa_uses_dynamic_stack 0
		.amdhsa_enable_private_segment 0
		.amdhsa_system_sgpr_workgroup_id_x 1
		.amdhsa_system_sgpr_workgroup_id_y 0
		.amdhsa_system_sgpr_workgroup_id_z 0
		.amdhsa_system_sgpr_workgroup_info 0
		.amdhsa_system_vgpr_workitem_id 0
		.amdhsa_next_free_vgpr 248
		.amdhsa_next_free_sgpr 98
		.amdhsa_accum_offset 248
		.amdhsa_reserve_vcc 1
		.amdhsa_float_round_mode_32 0
		.amdhsa_float_round_mode_16_64 0
		.amdhsa_float_denorm_mode_32 3
		.amdhsa_float_denorm_mode_16_64 3
		.amdhsa_dx10_clamp 1
		.amdhsa_ieee_mode 1
		.amdhsa_fp16_overflow 0
		.amdhsa_tg_split 0
		.amdhsa_exception_fp_ieee_invalid_op 0
		.amdhsa_exception_fp_denorm_src 0
		.amdhsa_exception_fp_ieee_div_zero 0
		.amdhsa_exception_fp_ieee_overflow 0
		.amdhsa_exception_fp_ieee_underflow 0
		.amdhsa_exception_fp_ieee_inexact 0
		.amdhsa_exception_int_div_zero 0
	.end_amdhsa_kernel

; __global__ void __launch_bounds__(NTHREADS, 2) fwd(Args args) {
amdhsa.kernels:
  - .agpr_count:     0
    .args:
      - .offset:         0
        .size:           256
        .value_kind:     by_value
      - .offset:         256
        .size:           4
        .value_kind:     hidden_block_count_x
      - .offset:         260
        .size:           4
        .value_kind:     hidden_block_count_y
      - .offset:         264
        .size:           4
        .value_kind:     hidden_block_count_z
      - .offset:         268
        .size:           2
        .value_kind:     hidden_group_size_x
      - .offset:         270
        .size:           2
        .value_kind:     hidden_group_size_y
      - .offset:         272
        .size:           2
        .value_kind:     hidden_group_size_z
      - .offset:         274
        .size:           2
        .value_kind:     hidden_remainder_x
      - .offset:         276
        .size:           2
        .value_kind:     hidden_remainder_y
      - .offset:         278
        .size:           2
        .value_kind:     hidden_remainder_z
      - .offset:         296
        .size:           8
        .value_kind:     hidden_global_offset_x
      - .offset:         304
        .size:           8
        .value_kind:     hidden_global_offset_y
      - .offset:         312
        .size:           8
        .value_kind:     hidden_global_offset_z
      - .offset:         320
        .size:           2
        .value_kind:     hidden_grid_dims
      - .offset:         376
        .size:           4
        .value_kind:     hidden_dynamic_lds_size
    .group_segment_fixed_size: 0
    .kernarg_segment_align: 8
    .kernarg_segment_size: 512
    .language:       OpenCL C
    .language_version:
      - 2
      - 0
    .max_flat_workgroup_size: 512
    .name:           _Z3fwd4Args
    .private_segment_fixed_size: 0
    .sgpr_count:     104
    .sgpr_spill_count: 47
    .symbol:         _Z3fwd4Args.kd
    .uniform_work_group_size: 1
    .uses_dynamic_stack: false
    .vgpr_count:     248
    .vgpr_spill_count: 0
    .wavefront_size: 64
